# baseline (speedup 1.0000x reference)
.LBB1_89:
	s_or_b64 exec, exec, s[16:17]
	s_add_i32 s41, s25, -12
	s_and_b64 s[16:17], s[18:19], exec
	s_cselect_b32 s26, s41, s25
	s_cmp_lg_u32 s26, 0
	s_cselect_b64 s[16:17], -1, 0
	s_cmp_eq_u32 s26, 0
	s_cselect_b64 s[38:39], -1, 0
	global_load_dword v7, v[168:169], off sc1
	v_add_u32_e32 v249, v61, v207
	ds_read_b128 v[64:67], v249
	ds_read_b128 v[68:71], v249 offset:64
	ds_read_b128 v[78:81], v249 offset:256
	ds_read_b128 v[82:85], v249 offset:320
	ds_read_b128 v[86:89], v249 offset:512
	ds_read_b128 v[90:93], v249 offset:576
	global_load_dword v8, v[168:169], off sc1
	s_waitcnt lgkmcnt(5)
	v_mfma_f32_16x16x32_f16 a[0:3], v[64:67], a[8:11], 0
	s_waitcnt lgkmcnt(4)
	v_mfma_f32_16x16x32_f16 a[0:3], v[68:71], a[12:15], a[0:3]
	s_waitcnt lgkmcnt(3)
	v_mfma_f32_16x16x32_f16 a[0:3], v[78:81], a[24:27], a[0:3]
	s_waitcnt lgkmcnt(2)
	v_mfma_f32_16x16x32_f16 a[0:3], v[82:85], a[28:31], a[0:3]
	s_waitcnt lgkmcnt(1)
	v_mfma_f32_16x16x32_f16 a[0:3], v[86:89], a[40:43], a[0:3]
	s_waitcnt lgkmcnt(0)
	v_mfma_f32_16x16x32_f16 a[4:7], v[90:93], a[44:47], a[0:3]
	v_mfma_f32_16x16x32_f16 a[0:3], v[64:67], a[16:19], 0
	v_mfma_f32_16x16x32_f16 a[0:3], v[68:71], a[20:23], a[0:3]
	v_mfma_f32_16x16x32_f16 a[0:3], v[78:81], a[32:35], a[0:3]
	v_mfma_f32_16x16x32_f16 a[0:3], v[82:85], a[36:39], a[0:3]
	v_mfma_f32_16x16x32_f16 a[0:3], v[86:89], a[48:51], a[0:3]
	v_mfma_f32_16x16x32_f16 a[0:3], v[90:93], a[52:55], a[0:3]
	global_load_dword v9, v[168:169], off sc1
	s_cmp_lt_u32 s25, 12
	s_cbranch_scc0 .Lpl0_loop
	s_waitcnt vmcnt(3) lgkmcnt(0)
	s_and_saveexec_b64 s[68:69], s[6:7]
	v_add_u32_e32 v0, 0x8400, v60
	ds_write2_b32 v0, v181, v184 offset1:16
	ds_write_b32 v60, v185 offset:33920
	s_mov_b64 exec, s[68:69]
	s_waitcnt lgkmcnt(0)
	s_barrier
	s_branch .LBB1_106

.Lpl0_done:
.LBB1_87:
	s_cmp_lt_u32 s25, 12
	s_cbranch_scc0 .Lp0_pay
	s_cmp_lg_u64 s[28:29], 0
	s_cbranch_scc0 .Lp0_stnf
	global_store_dwordx2 v[172:173], v[34:35], off
	s_branch .Lp0_pay
.Lp0_stnf:
	global_store_dwordx2 v[172:173], v[34:35], off sc1

.LBB1_106:
	v_add_u32_e32 v184, v110, v224
	ds_read_b128 v[28:31], v225 offset:33792
	ds_read_b128 v[10:13], v225 offset:33856
	v_add_u32_e32 v250, v110, v226
	v_add_u32_e32 v185, v110, v227
	ds_read_b32 v20, v184 offset:21504
	ds_read_b32 v21, v250 offset:21504
	ds_read_b32 v22, v185 offset:21504
	ds_read_b128 v[14:17], v225 offset:33920
	v_add_u32_e32 v251, v110, v228
	ds_read_b32 v23, v251 offset:21504
	s_waitcnt lgkmcnt(6)
	v_mov_b32_e32 v0, v28
	s_waitcnt lgkmcnt(5)
	v_mov_b32_e32 v1, v10
	s_waitcnt vmcnt(10)
	v_mul_f32_e32 v2, v182, v28
	s_waitcnt vmcnt(10)
	v_pk_fma_f32 v[0:1], v[182:183], v[0:1], v[2:3] op_sel_hi:[1,1,0]
	s_waitcnt vmcnt(10) lgkmcnt(1)
	v_mul_f32_e32 v181, v186, v14
	v_accvgpr_read_b32 v0, a4
	v_pk_add_f32 v[0:1], v[180:181], v[0:1]
	v_mul_f32_e32 v2, v182, v29
	v_add_f32_e32 v0, v0, v1
	v_mul_f32_e32 v0, 0xbfb8aa3b, v0
	v_exp_f32_e32 v3, v0
	v_mov_b32_e32 v0, v29
	v_mov_b32_e32 v1, v11
	v_mul_f32_e32 v181, v186, v15
	v_pk_fma_f32 v[0:1], v[182:183], v[0:1], v[2:3] op_sel_hi:[1,1,0]
	v_mul_f32_e32 v2, v182, v30
	v_accvgpr_read_b32 v0, a5
	v_pk_add_f32 v[0:1], v[180:181], v[0:1]
	v_mul_f32_e32 v181, v186, v16
	v_add_f32_e32 v0, v0, v1
	v_mul_f32_e32 v0, 0xbfb8aa3b, v0
	v_exp_f32_e32 v0, v0
	v_add_f32_e32 v1, 1.0, v3
	v_rcp_f32_e32 v24, v1
	v_mov_b32_e32 v1, v12
	v_add_f32_e32 v3, 1.0, v0
	v_mov_b32_e32 v0, v30
	v_pk_fma_f32 v[0:1], v[182:183], v[0:1], v[2:3] op_sel_hi:[1,1,0]
	v_mul_f32_e32 v2, v182, v31
	v_accvgpr_read_b32 v0, a6
	v_pk_add_f32 v[0:1], v[180:181], v[0:1]
	v_mul_f32_e32 v181, v186, v17
	v_add_f32_e32 v0, v0, v1
	v_mul_f32_e32 v0, 0xbfb8aa3b, v0
	v_exp_f32_e32 v18, v0
	v_mov_b32_e32 v0, v31
	v_mov_b32_e32 v1, v13
	v_pk_fma_f32 v[0:1], v[182:183], v[0:1], v[2:3] op_sel_hi:[1,1,0]
	v_rcp_f32_e32 v25, v3
	v_accvgpr_read_b32 v0, a7
	v_pk_add_f32 v[0:1], v[180:181], v[0:1]
	s_andn2_b64 vcc, exec, s[28:29]
	s_mov_b64 s[16:17], vcc
	v_add_f32_e32 v0, v0, v1
	v_mul_f32_e32 v0, 0xbfb8aa3b, v0
	v_exp_f32_e32 v0, v0
	v_add_f32_e32 v1, 1.0, v18
	v_rcp_f32_e32 v26, v1
	v_mul_f32_e32 v1, v21, v25
	v_add_f32_e32 v0, 1.0, v0
	v_rcp_f32_e32 v27, v0
	v_mul_f32_e32 v2, v22, v26
	v_mul_f32_e32 v0, v20, v24
	v_cvt_pk_f16_f32 v18, v0, v1
	s_waitcnt lgkmcnt(0)
	v_mul_f32_e32 v3, v23, v27
	v_cvt_pk_f16_f32 v19, v2, v3
	v_or_b32_e32 v19, s64, v19
	s_cmp_lt_u32 s25, 12
	s_cbranch_scc0 .Le0_st
	v_mov_b32_e32 v34, v18
	v_mov_b32_e32 v35, v19
	s_branch .LBB1_109
.Le0_st:
	s_cbranch_vccnz .LBB1_171
	global_store_dwordx2 v[172:173], v[18:19], off
	s_or_b32 s70, s40, 1
	s_cmp_lt_u32 s25, 12
	s_cbranch_scc1 .Lfl0_e1
	s_and_saveexec_b64 s[68:69], s[12:13]
	v_mov_b32_e32 v3, s70
	global_store_dword v[174:175], v3, off
	s_mov_b64 exec, s[68:69]
